# v12: inproj start stagger per workgroup group roughly halved (sleep 65 instead of 127 units)
# speedup vs baseline: 1.0219x; 1.0018x over previous
.LBB0_535:
	s_add_i32 s0, s0, -1
	s_cmp_eq_u32 s0, 0
	s_sleep 0x41
	s_cbranch_scc0 .LBB0_535
